# next-unit scheduling arithmetic moved under the epilogue bias wait / align barrier (P6, P7); P7 second-half bias slice loaded up front (no mid-epilogue drains)
# speedup vs baseline: 1.0399x; 1.0043x over previous
.Lp1_entry_pre:
	s_andn2_b64 vcc, exec, s[12:13]
	s_cbranch_vccnz .Lp1_entry
	s_barrier

.Lp3_entry_pre:
	s_andn2_b64 vcc, exec, s[10:11]
	s_cbranch_vccnz .Lp3_entry
	s_barrier

.LBB0_781:
	s_ashr_i32 s37, s36, 31
	v_lshl_or_b32 v20, s34, 7, v210
	s_lshl_b64 s[36:37], s[36:37], 13
	s_add_u32 s38, s48, s36
	v_ashrrev_i32_e32 v21, 31, v20
	s_addc_u32 s39, s49, s37
	v_lshlrev_b64 v[2:3], 2, v[20:21]
	v_lshl_add_u64 v[8:9], s[38:39], 0, v[2:3]
	global_load_dwordx4 v[4:7], v[8:9], off
	global_load_dwordx4 v[12:15], v[8:9], off offset:16
	s_add_u32 s36, s52, s36
	s_addc_u32 s37, s53, s37
	v_lshl_add_u64 v[2:3], s[36:37], 0, v[2:3]
	global_load_dwordx4 v[24:27], v[2:3], off
	global_load_dwordx4 v[28:31], v[2:3], off offset:16
	v_lshl_add_u32 v22, s82, 8, v207
	v_ashrrev_i32_e32 v23, 31, v22
	v_lshlrev_b64 v[2:3], 11, v[22:23]
	v_mov_b32_e32 v32, v163
	v_mov_b32_e32 v33, v163
	v_lshl_add_u64 v[2:3], s[14:15], 0, v[2:3]
	v_lshl_add_u64 v[2:3], v[2:3], 0, v[20:21]
	s_mov_b64 s[98:99], s[0:1]
	s_andn2_b64 vcc, exec, s[0:1]
	s_cbranch_vccnz .Lp6u_done
	v_mov_b32_e32 v178, v170
	v_mov_b32_e32 v176, v162
	v_mov_b32_e32 v182, v174
	v_mov_b32_e32 v180, v172
	s_mov_b32 s36, s28
	s_mov_b32 s34, s26
	s_mov_b32 s82, s80
	s_mov_b64 s[40:41], s[30:31]
	s_add_i32 s66, s66, 1
	s_mul_i32 s0, s66, s67
	s_mul_hi_u32 s1, s66, s94
	s_add_i32 s1, s1, s0
	s_mul_i32 s0, s66, s94
	v_readlane_b32 s27, v254, 18
	s_add_u32 s38, s0, s27
	s_addc_u32 s39, s1, s54
	v_cmp_lt_i64_e64 s[0:1], s[38:39], v[168:169]
	s_mov_b64 s[30:31], -1
	s_and_b64 vcc, exec, s[0:1]
	s_cbranch_vccnz .Lp6u_774
	s_ashr_i32 s29, s28, 31
	s_mov_b64 s[30:31], 0
.Lp6u_774:
	s_andn2_b64 vcc, exec, s[30:31]
	s_mov_b64 s[30:31], s[40:41]
	s_cbranch_vccnz .Lp6u_776
	s_ashr_i32 s26, s38, 31
	s_lshr_b32 s26, s26, 29
	s_add_i32 s26, s38, s26
	s_ashr_i32 s27, s26, 3
	s_and_b32 s26, s26, -8
	s_sub_i32 s26, s38, s26
	s_cmp_lt_i32 s26, 0
	s_cselect_b32 s28, s25, s23
	s_mul_i32 s26, s26, s28
	s_add_i32 s26, s26, s27
	s_ashr_i32 s27, s26, 31
	s_lshr_b32 s27, s27, 25
	s_add_i32 s27, s26, s27
	s_ashr_i32 s28, s27, 7
	s_lshl_b32 s28, s28, 3
	s_sub_i32 s29, s21, s28
	s_min_i32 s29, s29, 8
	s_abs_i32 s30, s29
	v_cvt_f32_u32_e32 v16, s30
	s_sub_i32 s37, 0, s30
	s_and_b32 s27, s27, 0xffffff80
	s_sub_i32 s27, s26, s27
	v_rcp_iflag_f32_e32 v16, v16
	s_abs_i32 s26, s27
	s_xor_b32 s31, s27, s29
	s_ashr_i32 s31, s31, 31
	v_mul_f32_e32 v16, 0x4f7ffffe, v16
	v_cvt_u32_f32_e32 v16, v16
	s_nop 0
	v_readfirstlane_b32 s38, v16
	s_mul_i32 s37, s37, s38
	s_mul_hi_u32 s37, s38, s37
	s_add_i32 s38, s38, s37
	s_mul_hi_u32 s37, s26, s38
	s_mul_i32 s38, s37, s30
	s_sub_i32 s26, s26, s38
	s_add_i32 s39, s37, 1
	s_sub_i32 s38, s26, s30
	s_cmp_ge_u32 s26, s30
	s_cselect_b32 s37, s39, s37
	s_cselect_b32 s26, s38, s26
	s_add_i32 s38, s37, 1
	s_cmp_ge_u32 s26, s30
	s_cselect_b32 s26, s38, s37
	s_xor_b32 s26, s26, s31
	s_sub_i32 s26, s26, s31
	s_mul_i32 s29, s26, s29
	s_sub_i32 s27, s27, s29
	s_add_i32 s80, s28, s27
	s_add_i32 s27, s80, 0
	s_add_i32 s27, s27, 0x22200
	v_mov_b32_e32 v16, s27
	ds_read_u8 v16, v16
	s_waitcnt lgkmcnt(0)
	v_readfirstlane_b32 s28, v16
	s_lshl_b32 s27, s28, 2
	s_add_i32 s27, s27, 0
	s_add_i32 s27, s27, 0x22040
	v_mov_b32_e32 v16, s27
	ds_read_b32 v16, v16
	s_ashr_i32 s29, s28, 31
	s_lshl_b64 s[30:31], s[28:29], 23
	s_waitcnt lgkmcnt(0)
	v_readfirstlane_b32 s27, v16
	s_sub_i32 s81, s80, s27
	s_add_u32 s37, s46, s30
	s_addc_u32 s38, s47, s31
	s_ashr_i32 s27, s26, 31
	s_lshl_b64 s[30:31], s[26:27], 19
	s_add_u32 s30, s37, s30
	s_addc_u32 s31, s38, s31
.Lp6u_776:
	s_lshl_b32 s27, s81, 8
	v_or_b32_e32 v214, s27, v1
	v_or_b32_e32 v216, s27, v204
	s_lshl_b32 s27, s28, 2
	s_add_i32 s27, s27, 0
	s_lshl_b64 s[38:39], s[28:29], 16
	s_add_i32 s27, s27, 0x22100
	s_add_u32 s38, s50, s38
	s_addc_u32 s39, s51, s39
	v_mov_b32_e32 v177, v163
	v_mov_b32_e32 v179, v163
	v_mov_b32_e32 v181, v163
	v_mov_b32_e32 v183, v163
	s_add_u32 s29, s40, 0x100
	v_or_b32_e32 v215, 0x80, v214
	v_or_b32_e32 v217, 0x80, v216
	v_lshl_add_u64 v[184:185], s[18:19], 0, v[182:183]
	v_lshl_add_u64 v[186:187], s[18:19], 0, v[180:181]
	v_lshl_add_u64 v[188:189], s[18:19], 0, v[178:179]
	v_lshl_add_u64 v[190:191], s[18:19], 0, v[176:177]
	s_addc_u32 s37, s41, 0
	s_mov_b32 s83, -2
	s_mov_b64 s[40:41], 0

.LBB0_783:
	s_nop 15
	s_nop 15
	s_waitcnt vmcnt(0)
	v_pk_mul_f32 v[8:9], v[6:7], s[20:21] op_sel_hi:[1,0]
	v_pk_mul_f32 v[10:11], v[4:5], s[20:21] op_sel_hi:[1,0]
	v_pk_mul_f32 v[6:7], v[12:13], s[20:21] op_sel_hi:[1,0]
	v_pk_mul_f32 v[4:5], v[14:15], s[20:21] op_sel_hi:[1,0]
	v_pk_fma_f32 v[158:159], v[158:159], s[22:23], v[10:11] op_sel_hi:[1,0,1]
	v_pk_fma_f32 v[154:155], v[154:155], s[22:23], v[6:7] op_sel_hi:[1,0,1]
	v_pk_fma_f32 v[156:157], v[156:157], s[22:23], v[4:5] op_sel_hi:[1,0,1]
	v_pk_add_f32 v[16:17], v[26:27], 1.0 op_sel_hi:[1,0]
	v_pk_add_f32 v[18:19], v[24:25], 1.0 op_sel_hi:[1,0]
	v_min_f32_e32 v24, 0x42600000, v158
	v_min_f32_e32 v26, 0x42600000, v154
	v_min_f32_e32 v25, 0x42600000, v159
	v_min_f32_e32 v27, 0x42600000, v155
	v_pk_add_f32 v[12:13], v[30:31], 1.0 op_sel_hi:[1,0]
	v_min_f32_e32 v31, 0x42600000, v157
	v_mul_f32_e32 v23, 0xbe9d265f, v24
	v_mul_f32_e32 v155, 0xbe9d265f, v26
	v_mul_f32_e32 v157, 0xbe9d265f, v25
	v_mul_f32_e32 v158, 0xbe9d265f, v27
	v_min_f32_e32 v30, 0x42600000, v156
	v_exp_f32_e32 v154, v23
	v_exp_f32_e32 v156, v155
	v_exp_f32_e32 v155, v157
	v_exp_f32_e32 v157, v158
	v_pk_fma_f32 v[160:161], v[160:161], s[22:23], v[8:9] op_sel_hi:[1,0,1]
	v_pk_add_f32 v[14:15], v[28:29], 1.0 op_sel_hi:[1,0]
	v_min_f32_e32 v28, 0x42600000, v160
	v_min_f32_e32 v29, 0x42600000, v161
	v_pk_fma_f32 v[144:145], v[144:145], s[24:25], v[16:17] op_sel_hi:[1,0,1]
	v_pk_fma_f32 v[140:141], v[140:141], s[24:25], v[12:13] op_sel_hi:[1,0,1]
	v_mul_f32_e32 v159, 0xbe9d265f, v28
	v_mul_f32_e32 v160, 0xbe9d265f, v30
	v_mul_f32_e32 v161, 0xbe9d265f, v29
	v_mul_f32_e32 v171, 0xbe9d265f, v31
	v_med3_f32 v144, v144, s76, v213
	v_med3_f32 v140, v140, s76, v213
	v_med3_f32 v145, v145, s76, v213
	v_med3_f32 v141, v141, s76, v213
	v_exp_f32_e32 v158, v159
	v_exp_f32_e32 v160, v160
	v_exp_f32_e32 v159, v161
	v_exp_f32_e32 v161, v171
	v_pk_mul_f32 v[28:29], v[28:29], v[144:145]
	v_pk_mul_f32 v[30:31], v[30:31], v[140:141]
	v_pk_add_f32 v[140:141], v[154:155], 1.0 op_sel_hi:[1,0]
	v_pk_add_f32 v[144:145], v[156:157], 1.0 op_sel_hi:[1,0]
	v_rcp_f32_e32 v140, v140
	v_rcp_f32_e32 v144, v144
	v_rcp_f32_e32 v141, v141
	v_rcp_f32_e32 v145, v145
	v_pk_fma_f32 v[142:143], v[142:143], s[24:25], v[18:19] op_sel_hi:[1,0,1]
	v_pk_fma_f32 v[138:139], v[138:139], s[24:25], v[14:15] op_sel_hi:[1,0,1]
	v_med3_f32 v142, v142, s76, v213
	v_med3_f32 v138, v138, s76, v213
	v_med3_f32 v143, v143, s76, v213
	v_med3_f32 v139, v139, s76, v213
	v_pk_mul_f32 v[24:25], v[24:25], v[142:143]
	v_pk_mul_f32 v[26:27], v[26:27], v[138:139]
	v_pk_add_f32 v[138:139], v[158:159], 1.0 op_sel_hi:[1,0]
	v_pk_add_f32 v[142:143], v[160:161], 1.0 op_sel_hi:[1,0]
	v_rcp_f32_e32 v138, v138
	v_rcp_f32_e32 v142, v142
	v_rcp_f32_e32 v139, v139
	v_rcp_f32_e32 v143, v143
	v_pk_mul_f32 v[24:25], v[24:25], v[140:141]
	v_pk_mul_f32 v[26:27], v[26:27], v[144:145]
	v_cvt_pk_fp8_f32 v32, v24, v25
	v_cvt_pk_fp8_f32 v33, v26, v27
	v_pk_mul_f32 v[24:25], v[28:29], v[138:139]
	v_pk_mul_f32 v[26:27], v[30:31], v[142:143]
	v_cvt_pk_fp8_f32 v32, v24, v25 op_sel:[0,0,1]
	v_cvt_pk_fp8_f32 v33, v26, v27 op_sel:[0,0,1]
	v_pk_fma_f32 v[152:153], v[152:153], s[22:23], v[8:9] op_sel_hi:[1,0,1]
	v_pk_fma_f32 v[150:151], v[150:151], s[22:23], v[10:11] op_sel_hi:[1,0,1]
	v_pk_fma_f32 v[148:149], v[148:149], s[22:23], v[4:5] op_sel_hi:[1,0,1]
	v_pk_fma_f32 v[146:147], v[146:147], s[22:23], v[6:7] op_sel_hi:[1,0,1]
	v_min_f32_e32 v150, 0x42600000, v150
	v_pk_fma_f32 v[134:135], v[134:135], s[24:25], v[18:19] op_sel_hi:[1,0,1]
	v_min_f32_e32 v28, 0x42600000, v152
	v_min_f32_e32 v146, 0x42600000, v146
	v_pk_fma_f32 v[136:137], v[136:137], s[24:25], v[16:17] op_sel_hi:[1,0,1]
	v_pk_fma_f32 v[132:133], v[132:133], s[24:25], v[12:13] op_sel_hi:[1,0,1]
	v_med3_f32 v27, v135, s76, v213
	v_min_f32_e32 v30, 0x42600000, v148
	v_mul_f32_e32 v23, 0xbe9d265f, v150
	v_mul_f32_e32 v135, 0xbe9d265f, v28
	v_pk_fma_f32 v[24:25], v[130:131], s[24:25], v[14:15] op_sel_hi:[1,0,1]
	global_store_dwordx2 v[2:3], v[32:33], off
	v_min_f32_e32 v151, 0x42600000, v151
	v_med3_f32 v32, v136, s76, v213
	v_med3_f32 v130, v132, s76, v213
	v_min_f32_e32 v29, 0x42600000, v153
	v_exp_f32_e32 v132, v23
	v_mul_f32_e32 v23, 0xbe9d265f, v146
	v_exp_f32_e32 v136, v135
	v_mul_f32_e32 v135, 0xbe9d265f, v30
	v_med3_f32 v26, v134, s76, v213
	v_min_f32_e32 v147, 0x42600000, v147
	v_min_f32_e32 v31, 0x42600000, v149
	v_exp_f32_e32 v134, v23
	v_mul_f32_e32 v23, 0xbe9d265f, v151
	v_exp_f32_e32 v138, v135
	v_mul_f32_e32 v135, 0xbe9d265f, v29
	v_med3_f32 v33, v137, s76, v213
	v_med3_f32 v131, v133, s76, v213
	v_exp_f32_e32 v133, v23
	v_mul_f32_e32 v23, 0xbe9d265f, v147
	v_exp_f32_e32 v137, v135
	v_mul_f32_e32 v135, 0xbe9d265f, v31
	v_exp_f32_e32 v139, v135
	v_exp_f32_e32 v135, v23
	v_pk_add_f32 v[132:133], v[132:133], 1.0 op_sel_hi:[1,0]
	v_med3_f32 v24, v24, s76, v213
	v_rcp_f32_e32 v132, v132
	v_pk_add_f32 v[134:135], v[134:135], 1.0 op_sel_hi:[1,0]
	v_rcp_f32_e32 v133, v133
	v_rcp_f32_e32 v134, v134
	v_rcp_f32_e32 v135, v135
	v_med3_f32 v25, v25, s76, v213
	v_pk_add_f32 v[138:139], v[138:139], 1.0 op_sel_hi:[1,0]
	v_pk_mul_f32 v[24:25], v[146:147], v[24:25]
	v_pk_add_f32 v[136:137], v[136:137], 1.0 op_sel_hi:[1,0]
	v_rcp_f32_e32 v138, v138
	v_rcp_f32_e32 v139, v139
	v_pk_mul_f32 v[28:29], v[28:29], v[32:33]
	v_pk_mul_f32 v[26:27], v[150:151], v[26:27]
	v_pk_mul_f32 v[24:25], v[24:25], v[134:135]
	v_mov_b32_e32 v33, v163
	v_rcp_f32_e32 v136, v136
	v_rcp_f32_e32 v137, v137
	v_pk_mul_f32 v[26:27], v[26:27], v[132:133]
	v_mov_b32_e32 v32, v163
	v_cvt_pk_fp8_f32 v33, v24, v25
	v_cvt_pk_fp8_f32 v32, v26, v27
	v_pk_mul_f32 v[24:25], v[30:31], v[130:131]
	v_pk_mul_f32 v[28:29], v[28:29], v[136:137]
	v_pk_mul_f32 v[24:25], v[24:25], v[138:139]
	v_cvt_pk_fp8_f32 v32, v28, v29 op_sel:[0,0,1]
	v_cvt_pk_fp8_f32 v33, v24, v25 op_sel:[0,0,1]
	v_or_b32_e32 v24, 16, v22
	v_ashrrev_i32_e32 v25, 31, v24
	v_lshlrev_b64 v[24:25], 11, v[24:25]
	v_lshl_add_u64 v[24:25], s[14:15], 0, v[24:25]
	v_lshl_add_u64 v[24:25], v[24:25], 0, v[20:21]
	global_store_dwordx2 v[24:25], v[32:33], off
	v_pk_fma_f32 v[24:25], v[128:129], s[22:23], v[8:9] op_sel_hi:[1,0,1]
	v_pk_fma_f32 v[26:27], v[126:127], s[22:23], v[10:11] op_sel_hi:[1,0,1]
	v_pk_fma_f32 v[28:29], v[124:125], s[22:23], v[4:5] op_sel_hi:[1,0,1]
	v_pk_fma_f32 v[30:31], v[122:123], s[22:23], v[6:7] op_sel_hi:[1,0,1]
	v_min_f32_e32 v26, 0x42600000, v26
	v_min_f32_e32 v24, 0x42600000, v24
	v_min_f32_e32 v30, 0x42600000, v30
	v_min_f32_e32 v28, 0x42600000, v28
	v_mul_f32_e32 v23, 0xbe9d265f, v26
	v_mul_f32_e32 v123, 0xbe9d265f, v24
	v_pk_fma_f32 v[32:33], v[120:121], s[24:25], v[16:17] op_sel_hi:[1,0,1]
	v_min_f32_e32 v27, 0x42600000, v27
	v_min_f32_e32 v25, 0x42600000, v25
	v_exp_f32_e32 v120, v23
	v_mul_f32_e32 v23, 0xbe9d265f, v30
	v_exp_f32_e32 v124, v123
	v_mul_f32_e32 v123, 0xbe9d265f, v28
	v_min_f32_e32 v31, 0x42600000, v31
	v_min_f32_e32 v29, 0x42600000, v29
	v_exp_f32_e32 v122, v23
	v_mul_f32_e32 v23, 0xbe9d265f, v27
	v_exp_f32_e32 v126, v123
	v_mul_f32_e32 v123, 0xbe9d265f, v25
	v_exp_f32_e32 v121, v23
	v_mul_f32_e32 v23, 0xbe9d265f, v31
	v_exp_f32_e32 v125, v123
	v_mul_f32_e32 v123, 0xbe9d265f, v29
	v_exp_f32_e32 v127, v123
	v_exp_f32_e32 v123, v23
	v_pk_add_f32 v[120:121], v[120:121], 1.0 op_sel_hi:[1,0]
	v_pk_fma_f32 v[118:119], v[118:119], s[24:25], v[18:19] op_sel_hi:[1,0,1]
	v_rcp_f32_e32 v120, v120
	v_pk_add_f32 v[122:123], v[122:123], 1.0 op_sel_hi:[1,0]
	v_rcp_f32_e32 v121, v121
	v_rcp_f32_e32 v122, v122
	v_rcp_f32_e32 v123, v123
	v_pk_fma_f32 v[114:115], v[114:115], s[24:25], v[14:15] op_sel_hi:[1,0,1]
	v_med3_f32 v118, v118, s76, v213
	v_med3_f32 v119, v119, s76, v213
	v_med3_f32 v114, v114, s76, v213
	v_med3_f32 v115, v115, s76, v213
	v_med3_f32 v32, v32, s76, v213
	v_med3_f32 v33, v33, s76, v213
	v_pk_add_f32 v[124:125], v[124:125], 1.0 op_sel_hi:[1,0]
	v_pk_mul_f32 v[26:27], v[26:27], v[118:119]
	v_pk_add_f32 v[126:127], v[126:127], 1.0 op_sel_hi:[1,0]
	v_rcp_f32_e32 v124, v124
	v_rcp_f32_e32 v125, v125
	v_pk_mul_f32 v[24:25], v[24:25], v[32:33]
	v_pk_mul_f32 v[26:27], v[26:27], v[120:121]
	v_pk_mul_f32 v[30:31], v[30:31], v[114:115]
	v_mov_b32_e32 v32, v163
	v_rcp_f32_e32 v126, v126
	v_rcp_f32_e32 v127, v127
	v_pk_mul_f32 v[30:31], v[30:31], v[122:123]
	v_cvt_pk_fp8_f32 v32, v26, v27
	v_mov_b32_e32 v33, v163
	v_pk_fma_f32 v[116:117], v[116:117], s[24:25], v[12:13] op_sel_hi:[1,0,1]
	v_cvt_pk_fp8_f32 v33, v30, v31
	v_med3_f32 v116, v116, s76, v213
	v_med3_f32 v117, v117, s76, v213
	v_pk_mul_f32 v[24:25], v[24:25], v[124:125]
	v_pk_mul_f32 v[26:27], v[28:29], v[116:117]
	v_cvt_pk_fp8_f32 v32, v24, v25 op_sel:[0,0,1]
	v_pk_mul_f32 v[26:27], v[26:27], v[126:127]
	v_or_b32_e32 v24, 32, v22
	v_cvt_pk_fp8_f32 v33, v26, v27 op_sel:[0,0,1]
	v_ashrrev_i32_e32 v25, 31, v24
	v_lshlrev_b64 v[24:25], 11, v[24:25]
	v_lshl_add_u64 v[24:25], s[14:15], 0, v[24:25]
	v_lshl_add_u64 v[24:25], v[24:25], 0, v[20:21]
	global_store_dwordx2 v[24:25], v[32:33], off
	v_pk_fma_f32 v[24:25], v[112:113], s[22:23], v[8:9] op_sel_hi:[1,0,1]
	v_pk_fma_f32 v[26:27], v[110:111], s[22:23], v[10:11] op_sel_hi:[1,0,1]
	v_pk_fma_f32 v[28:29], v[108:109], s[22:23], v[4:5] op_sel_hi:[1,0,1]
	v_pk_fma_f32 v[30:31], v[106:107], s[22:23], v[6:7] op_sel_hi:[1,0,1]
	v_min_f32_e32 v26, 0x42600000, v26
	v_min_f32_e32 v24, 0x42600000, v24
	v_min_f32_e32 v30, 0x42600000, v30
	v_min_f32_e32 v28, 0x42600000, v28
	v_mul_f32_e32 v23, 0xbe9d265f, v26
	v_mul_f32_e32 v107, 0xbe9d265f, v24
	v_pk_fma_f32 v[32:33], v[104:105], s[24:25], v[16:17] op_sel_hi:[1,0,1]
	v_min_f32_e32 v27, 0x42600000, v27
	v_min_f32_e32 v25, 0x42600000, v25
	v_exp_f32_e32 v104, v23
	v_mul_f32_e32 v23, 0xbe9d265f, v30
	v_exp_f32_e32 v108, v107
	v_mul_f32_e32 v107, 0xbe9d265f, v28
	v_min_f32_e32 v31, 0x42600000, v31
	v_min_f32_e32 v29, 0x42600000, v29
	v_exp_f32_e32 v106, v23
	v_mul_f32_e32 v23, 0xbe9d265f, v27
	v_exp_f32_e32 v110, v107
	v_mul_f32_e32 v107, 0xbe9d265f, v25
	v_exp_f32_e32 v105, v23
	v_mul_f32_e32 v23, 0xbe9d265f, v31
	v_exp_f32_e32 v109, v107
	v_mul_f32_e32 v107, 0xbe9d265f, v29
	v_exp_f32_e32 v111, v107
	v_exp_f32_e32 v107, v23
	v_pk_add_f32 v[104:105], v[104:105], 1.0 op_sel_hi:[1,0]
	v_pk_fma_f32 v[102:103], v[102:103], s[24:25], v[18:19] op_sel_hi:[1,0,1]
	v_rcp_f32_e32 v104, v104
	v_pk_add_f32 v[106:107], v[106:107], 1.0 op_sel_hi:[1,0]
	v_rcp_f32_e32 v105, v105
	v_rcp_f32_e32 v106, v106
	v_rcp_f32_e32 v107, v107
	v_pk_fma_f32 v[98:99], v[98:99], s[24:25], v[14:15] op_sel_hi:[1,0,1]
	v_med3_f32 v102, v102, s76, v213
	v_med3_f32 v98, v98, s76, v213
	v_med3_f32 v103, v103, s76, v213
	v_med3_f32 v99, v99, s76, v213
	v_med3_f32 v32, v32, s76, v213
	v_med3_f32 v33, v33, s76, v213
	v_pk_add_f32 v[108:109], v[108:109], 1.0 op_sel_hi:[1,0]
	v_pk_add_f32 v[110:111], v[110:111], 1.0 op_sel_hi:[1,0]
	v_pk_mul_f32 v[26:27], v[26:27], v[102:103]
	v_pk_mul_f32 v[30:31], v[30:31], v[98:99]
	v_rcp_f32_e32 v108, v108
	v_rcp_f32_e32 v110, v110
	v_rcp_f32_e32 v109, v109
	v_rcp_f32_e32 v111, v111
	v_pk_mul_f32 v[24:25], v[24:25], v[32:33]
	v_pk_mul_f32 v[26:27], v[26:27], v[104:105]
	v_pk_mul_f32 v[30:31], v[30:31], v[106:107]
	v_mov_b32_e32 v32, v163
	v_mov_b32_e32 v33, v163
	v_pk_fma_f32 v[100:101], v[100:101], s[24:25], v[12:13] op_sel_hi:[1,0,1]
	v_cvt_pk_fp8_f32 v32, v26, v27
	v_cvt_pk_fp8_f32 v33, v30, v31
	v_med3_f32 v100, v100, s76, v213
	v_med3_f32 v101, v101, s76, v213
	v_pk_mul_f32 v[26:27], v[28:29], v[100:101]
	v_pk_mul_f32 v[24:25], v[24:25], v[108:109]
	v_pk_mul_f32 v[26:27], v[26:27], v[110:111]
	v_or_b32_e32 v22, 48, v22
	v_cvt_pk_fp8_f32 v32, v24, v25 op_sel:[0,0,1]
	v_cvt_pk_fp8_f32 v33, v26, v27 op_sel:[0,0,1]
	v_ashrrev_i32_e32 v23, 31, v22
	v_lshlrev_b64 v[22:23], 11, v[22:23]
	v_lshl_add_u64 v[22:23], s[14:15], 0, v[22:23]
	v_pk_fma_f32 v[26:27], v[90:91], s[22:23], v[6:7] op_sel_hi:[1,0,1]
	v_lshl_add_u64 v[20:21], v[22:23], 0, v[20:21]
	v_pk_fma_f32 v[22:23], v[94:95], s[22:23], v[10:11] op_sel_hi:[1,0,1]
	v_min_f32_e32 v26, 0x42600000, v26
	global_store_dwordx2 v[20:21], v[32:33], off
	v_pk_fma_f32 v[32:33], v[84:85], s[24:25], v[12:13] op_sel_hi:[1,0,1]
	v_min_f32_e32 v22, 0x42600000, v22
	v_min_f32_e32 v23, 0x42600000, v23
	v_min_f32_e32 v27, 0x42600000, v27
	v_mul_f32_e32 v85, 0xbe9d265f, v26
	v_pk_fma_f32 v[30:31], v[86:87], s[24:25], v[18:19] op_sel_hi:[1,0,1]
	v_mul_f32_e32 v84, 0xbe9d265f, v22
	v_exp_f32_e32 v86, v85
	v_mul_f32_e32 v85, 0xbe9d265f, v23
	v_mul_f32_e32 v87, 0xbe9d265f, v27
	v_pk_fma_f32 v[24:25], v[92:93], s[22:23], v[4:5] op_sel_hi:[1,0,1]
	v_exp_f32_e32 v84, v84
	v_exp_f32_e32 v85, v85
	v_exp_f32_e32 v87, v87
	v_pk_fma_f32 v[20:21], v[96:97], s[22:23], v[8:9] op_sel_hi:[1,0,1]
	v_min_f32_e32 v24, 0x42600000, v24
	v_pk_fma_f32 v[28:29], v[88:89], s[24:25], v[16:17] op_sel_hi:[1,0,1]
	v_min_f32_e32 v20, 0x42600000, v20
	v_min_f32_e32 v21, 0x42600000, v21
	v_min_f32_e32 v25, 0x42600000, v25
	v_mul_f32_e32 v89, 0xbe9d265f, v24
	v_mul_f32_e32 v88, 0xbe9d265f, v20
	v_exp_f32_e32 v90, v89
	v_mul_f32_e32 v89, 0xbe9d265f, v21
	v_mul_f32_e32 v91, 0xbe9d265f, v25
	v_exp_f32_e32 v88, v88
	v_exp_f32_e32 v89, v89
	v_exp_f32_e32 v91, v91
	v_pk_add_f32 v[84:85], v[84:85], 1.0 op_sel_hi:[1,0]
	v_pk_add_f32 v[86:87], v[86:87], 1.0 op_sel_hi:[1,0]
	v_rcp_f32_e32 v84, v84
	v_rcp_f32_e32 v86, v86
	v_rcp_f32_e32 v85, v85
	v_rcp_f32_e32 v87, v87
	v_pk_fma_f32 v[82:83], v[82:83], s[24:25], v[14:15] op_sel_hi:[1,0,1]
	v_med3_f32 v30, v30, s76, v213
	v_med3_f32 v82, v82, s76, v213
	v_med3_f32 v31, v31, s76, v213
	v_med3_f32 v83, v83, s76, v213
	v_med3_f32 v28, v28, s76, v213
	v_med3_f32 v29, v29, s76, v213
	v_pk_add_f32 v[88:89], v[88:89], 1.0 op_sel_hi:[1,0]
	v_pk_add_f32 v[90:91], v[90:91], 1.0 op_sel_hi:[1,0]
	v_pk_mul_f32 v[22:23], v[22:23], v[30:31]
	v_pk_mul_f32 v[26:27], v[26:27], v[82:83]
	v_rcp_f32_e32 v88, v88
	v_rcp_f32_e32 v90, v90
	v_rcp_f32_e32 v89, v89
	v_rcp_f32_e32 v91, v91
	v_pk_mul_f32 v[20:21], v[20:21], v[28:29]
	v_pk_mul_f32 v[22:23], v[22:23], v[84:85]
	v_pk_mul_f32 v[26:27], v[26:27], v[86:87]
	v_mov_b32_e32 v28, v163
	v_mov_b32_e32 v29, v163
	v_cvt_pk_fp8_f32 v28, v22, v23
	v_cvt_pk_fp8_f32 v29, v26, v27
	v_med3_f32 v32, v32, s76, v213
	v_med3_f32 v33, v33, s76, v213
	v_pk_mul_f32 v[22:23], v[24:25], v[32:33]
	v_pk_mul_f32 v[20:21], v[20:21], v[88:89]
	v_pk_mul_f32 v[22:23], v[22:23], v[90:91]
	v_pk_fma_f32 v[26:27], v[74:75], s[22:23], v[6:7] op_sel_hi:[1,0,1]
	v_cvt_pk_fp8_f32 v28, v20, v21 op_sel:[0,0,1]
	v_cvt_pk_fp8_f32 v29, v22, v23 op_sel:[0,0,1]
	v_pk_fma_f32 v[22:23], v[78:79], s[22:23], v[10:11] op_sel_hi:[1,0,1]
	v_min_f32_e32 v26, 0x42600000, v26
	v_pk_fma_f32 v[32:33], v[68:69], s[24:25], v[12:13] op_sel_hi:[1,0,1]
	v_min_f32_e32 v22, 0x42600000, v22
	v_min_f32_e32 v23, 0x42600000, v23
	v_min_f32_e32 v27, 0x42600000, v27
	v_mul_f32_e32 v69, 0xbe9d265f, v26
	v_add_co_u32_e32 v20, vcc, s77, v2
	v_pk_fma_f32 v[30:31], v[70:71], s[24:25], v[18:19] op_sel_hi:[1,0,1]
	v_mul_f32_e32 v68, 0xbe9d265f, v22
	v_exp_f32_e32 v70, v69
	v_mul_f32_e32 v69, 0xbe9d265f, v23
	v_mul_f32_e32 v71, 0xbe9d265f, v27
	v_addc_co_u32_e32 v21, vcc, 0, v3, vcc
	v_pk_fma_f32 v[24:25], v[76:77], s[22:23], v[4:5] op_sel_hi:[1,0,1]
	v_exp_f32_e32 v68, v68
	v_exp_f32_e32 v69, v69
	v_exp_f32_e32 v71, v71
	global_store_dwordx2 v[20:21], v[28:29], off
	v_pk_fma_f32 v[20:21], v[80:81], s[22:23], v[8:9] op_sel_hi:[1,0,1]
	v_min_f32_e32 v24, 0x42600000, v24
	v_pk_fma_f32 v[28:29], v[72:73], s[24:25], v[16:17] op_sel_hi:[1,0,1]
	v_min_f32_e32 v20, 0x42600000, v20
	v_min_f32_e32 v21, 0x42600000, v21
	v_min_f32_e32 v25, 0x42600000, v25
	v_mul_f32_e32 v73, 0xbe9d265f, v24
	v_mul_f32_e32 v72, 0xbe9d265f, v20
	v_exp_f32_e32 v74, v73
	v_mul_f32_e32 v73, 0xbe9d265f, v21
	v_mul_f32_e32 v75, 0xbe9d265f, v25
	v_exp_f32_e32 v72, v72
	v_exp_f32_e32 v73, v73
	v_exp_f32_e32 v75, v75
	v_pk_add_f32 v[68:69], v[68:69], 1.0 op_sel_hi:[1,0]
	v_pk_add_f32 v[70:71], v[70:71], 1.0 op_sel_hi:[1,0]
	v_rcp_f32_e32 v68, v68
	v_rcp_f32_e32 v70, v70
	v_rcp_f32_e32 v69, v69
	v_rcp_f32_e32 v71, v71
	v_pk_fma_f32 v[66:67], v[66:67], s[24:25], v[14:15] op_sel_hi:[1,0,1]
	v_med3_f32 v30, v30, s76, v213
	v_med3_f32 v66, v66, s76, v213
	v_med3_f32 v31, v31, s76, v213
	v_med3_f32 v67, v67, s76, v213
	v_med3_f32 v28, v28, s76, v213
	v_med3_f32 v29, v29, s76, v213
	v_pk_add_f32 v[72:73], v[72:73], 1.0 op_sel_hi:[1,0]
	v_pk_add_f32 v[74:75], v[74:75], 1.0 op_sel_hi:[1,0]
	v_pk_mul_f32 v[22:23], v[22:23], v[30:31]
	v_pk_mul_f32 v[26:27], v[26:27], v[66:67]
	v_rcp_f32_e32 v72, v72
	v_rcp_f32_e32 v74, v74
	v_rcp_f32_e32 v73, v73
	v_rcp_f32_e32 v75, v75
	v_pk_mul_f32 v[20:21], v[20:21], v[28:29]
	v_pk_mul_f32 v[22:23], v[22:23], v[68:69]
	v_pk_mul_f32 v[26:27], v[26:27], v[70:71]
	v_mov_b32_e32 v28, v163
	v_mov_b32_e32 v29, v163
	v_cvt_pk_fp8_f32 v28, v22, v23
	v_cvt_pk_fp8_f32 v29, v26, v27
	v_med3_f32 v32, v32, s76, v213
	v_med3_f32 v33, v33, s76, v213
	v_pk_mul_f32 v[22:23], v[24:25], v[32:33]
	v_pk_mul_f32 v[20:21], v[20:21], v[72:73]
	v_pk_mul_f32 v[22:23], v[22:23], v[74:75]
	v_pk_fma_f32 v[26:27], v[58:59], s[22:23], v[6:7] op_sel_hi:[1,0,1]
	v_cvt_pk_fp8_f32 v28, v20, v21 op_sel:[0,0,1]
	v_cvt_pk_fp8_f32 v29, v22, v23 op_sel:[0,0,1]
	v_pk_fma_f32 v[22:23], v[62:63], s[22:23], v[10:11] op_sel_hi:[1,0,1]
	v_min_f32_e32 v26, 0x42600000, v26
	v_pk_fma_f32 v[32:33], v[52:53], s[24:25], v[12:13] op_sel_hi:[1,0,1]
	v_min_f32_e32 v22, 0x42600000, v22
	v_min_f32_e32 v23, 0x42600000, v23
	v_min_f32_e32 v27, 0x42600000, v27
	v_mul_f32_e32 v53, 0xbe9d265f, v26
	v_add_co_u32_e32 v20, vcc, s78, v2
	v_pk_fma_f32 v[30:31], v[54:55], s[24:25], v[18:19] op_sel_hi:[1,0,1]
	v_mul_f32_e32 v52, 0xbe9d265f, v22
	v_exp_f32_e32 v54, v53
	v_mul_f32_e32 v53, 0xbe9d265f, v23
	v_mul_f32_e32 v55, 0xbe9d265f, v27
	v_addc_co_u32_e32 v21, vcc, 0, v3, vcc
	v_pk_fma_f32 v[24:25], v[60:61], s[22:23], v[4:5] op_sel_hi:[1,0,1]
	v_exp_f32_e32 v52, v52
	v_exp_f32_e32 v53, v53
	v_exp_f32_e32 v55, v55
	global_store_dwordx2 v[20:21], v[28:29], off
	v_pk_fma_f32 v[20:21], v[64:65], s[22:23], v[8:9] op_sel_hi:[1,0,1]
	v_min_f32_e32 v24, 0x42600000, v24
	v_pk_fma_f32 v[28:29], v[56:57], s[24:25], v[16:17] op_sel_hi:[1,0,1]
	v_min_f32_e32 v20, 0x42600000, v20
	v_min_f32_e32 v21, 0x42600000, v21
	v_min_f32_e32 v25, 0x42600000, v25
	v_mul_f32_e32 v57, 0xbe9d265f, v24
	v_mul_f32_e32 v56, 0xbe9d265f, v20
	v_exp_f32_e32 v58, v57
	v_mul_f32_e32 v57, 0xbe9d265f, v21
	v_mul_f32_e32 v59, 0xbe9d265f, v25
	v_exp_f32_e32 v56, v56
	v_exp_f32_e32 v57, v57
	v_exp_f32_e32 v59, v59
	v_pk_add_f32 v[52:53], v[52:53], 1.0 op_sel_hi:[1,0]
	v_pk_add_f32 v[54:55], v[54:55], 1.0 op_sel_hi:[1,0]
	v_rcp_f32_e32 v52, v52
	v_rcp_f32_e32 v54, v54
	v_rcp_f32_e32 v53, v53
	v_rcp_f32_e32 v55, v55
	v_pk_fma_f32 v[50:51], v[50:51], s[24:25], v[14:15] op_sel_hi:[1,0,1]
	v_med3_f32 v30, v30, s76, v213
	v_med3_f32 v50, v50, s76, v213
	v_med3_f32 v31, v31, s76, v213
	v_med3_f32 v51, v51, s76, v213
	v_med3_f32 v28, v28, s76, v213
	v_med3_f32 v29, v29, s76, v213
	v_pk_add_f32 v[56:57], v[56:57], 1.0 op_sel_hi:[1,0]
	v_pk_add_f32 v[58:59], v[58:59], 1.0 op_sel_hi:[1,0]
	v_pk_mul_f32 v[22:23], v[22:23], v[30:31]
	v_pk_mul_f32 v[26:27], v[26:27], v[50:51]
	v_rcp_f32_e32 v56, v56
	v_rcp_f32_e32 v58, v58
	v_rcp_f32_e32 v57, v57
	v_rcp_f32_e32 v59, v59
	v_pk_mul_f32 v[20:21], v[20:21], v[28:29]
	v_pk_mul_f32 v[22:23], v[22:23], v[52:53]
	v_pk_mul_f32 v[26:27], v[26:27], v[54:55]
	v_mov_b32_e32 v28, v163
	v_mov_b32_e32 v29, v163
	v_cvt_pk_fp8_f32 v28, v22, v23
	v_cvt_pk_fp8_f32 v29, v26, v27
	v_med3_f32 v32, v32, s76, v213
	v_med3_f32 v33, v33, s76, v213
	v_pk_mul_f32 v[22:23], v[24:25], v[32:33]
	v_pk_mul_f32 v[20:21], v[20:21], v[56:57]
	v_pk_mul_f32 v[22:23], v[22:23], v[58:59]
	v_cvt_pk_fp8_f32 v28, v20, v21 op_sel:[0,0,1]
	v_cvt_pk_fp8_f32 v29, v22, v23 op_sel:[0,0,1]
	v_add_co_u32_e32 v20, vcc, s79, v2
	v_pk_fma_f32 v[6:7], v[42:43], s[22:23], v[6:7] op_sel_hi:[1,0,1]
	s_nop 0
	v_addc_co_u32_e32 v21, vcc, 0, v3, vcc
	v_pk_fma_f32 v[10:11], v[46:47], s[22:23], v[10:11] op_sel_hi:[1,0,1]
	v_min_f32_e32 v6, 0x42600000, v6
	global_store_dwordx2 v[20:21], v[28:29], off
	v_min_f32_e32 v10, 0x42600000, v10
	v_min_f32_e32 v11, 0x42600000, v11
	v_min_f32_e32 v7, 0x42600000, v7
	v_mul_f32_e32 v21, 0xbe9d265f, v6
	v_mul_f32_e32 v20, 0xbe9d265f, v10
	v_exp_f32_e32 v22, v21
	v_mul_f32_e32 v21, 0xbe9d265f, v11
	v_mul_f32_e32 v23, 0xbe9d265f, v7
	v_pk_fma_f32 v[4:5], v[44:45], s[22:23], v[4:5] op_sel_hi:[1,0,1]
	v_exp_f32_e32 v20, v20
	v_exp_f32_e32 v21, v21
	v_exp_f32_e32 v23, v23
	v_pk_fma_f32 v[8:9], v[48:49], s[22:23], v[8:9] op_sel_hi:[1,0,1]
	v_min_f32_e32 v4, 0x42600000, v4
	v_min_f32_e32 v8, 0x42600000, v8
	v_min_f32_e32 v9, 0x42600000, v9
	v_min_f32_e32 v5, 0x42600000, v5
	v_mul_f32_e32 v25, 0xbe9d265f, v4
	v_mul_f32_e32 v24, 0xbe9d265f, v8
	v_exp_f32_e32 v26, v25
	v_mul_f32_e32 v25, 0xbe9d265f, v9
	v_mul_f32_e32 v27, 0xbe9d265f, v5
	v_exp_f32_e32 v24, v24
	v_exp_f32_e32 v25, v25
	v_exp_f32_e32 v27, v27
	v_pk_add_f32 v[20:21], v[20:21], 1.0 op_sel_hi:[1,0]
	v_pk_add_f32 v[22:23], v[22:23], 1.0 op_sel_hi:[1,0]
	v_rcp_f32_e32 v20, v20
	v_rcp_f32_e32 v22, v22
	v_rcp_f32_e32 v21, v21
	v_rcp_f32_e32 v23, v23
	v_pk_fma_f32 v[18:19], v[38:39], s[24:25], v[18:19] op_sel_hi:[1,0,1]
	v_pk_fma_f32 v[14:15], v[34:35], s[24:25], v[14:15] op_sel_hi:[1,0,1]
	v_med3_f32 v18, v18, s76, v213
	v_med3_f32 v14, v14, s76, v213
	v_med3_f32 v19, v19, s76, v213
	v_med3_f32 v15, v15, s76, v213
	v_pk_add_f32 v[24:25], v[24:25], 1.0 op_sel_hi:[1,0]
	v_pk_add_f32 v[26:27], v[26:27], 1.0 op_sel_hi:[1,0]
	v_pk_mul_f32 v[10:11], v[10:11], v[18:19]
	v_pk_mul_f32 v[6:7], v[6:7], v[14:15]
	v_rcp_f32_e32 v24, v24
	v_rcp_f32_e32 v26, v26
	v_rcp_f32_e32 v25, v25
	v_rcp_f32_e32 v27, v27
	v_pk_mul_f32 v[10:11], v[10:11], v[20:21]
	v_pk_mul_f32 v[6:7], v[6:7], v[22:23]
	v_mov_b32_e32 v14, v163
	v_mov_b32_e32 v15, v163
	v_pk_fma_f32 v[16:17], v[40:41], s[24:25], v[16:17] op_sel_hi:[1,0,1]
	v_pk_fma_f32 v[12:13], v[36:37], s[24:25], v[12:13] op_sel_hi:[1,0,1]
	v_cvt_pk_fp8_f32 v14, v10, v11
	v_cvt_pk_fp8_f32 v15, v6, v7
	v_med3_f32 v16, v16, s76, v213
	v_med3_f32 v12, v12, s76, v213
	v_med3_f32 v17, v17, s76, v213
	v_med3_f32 v13, v13, s76, v213
	v_pk_mul_f32 v[8:9], v[8:9], v[16:17]
	v_pk_mul_f32 v[4:5], v[4:5], v[12:13]
	v_pk_mul_f32 v[8:9], v[8:9], v[24:25]
	v_pk_mul_f32 v[4:5], v[4:5], v[26:27]
	v_cvt_pk_fp8_f32 v14, v8, v9 op_sel:[0,0,1]
	v_cvt_pk_fp8_f32 v15, v4, v5 op_sel:[0,0,1]
	v_add_co_u32_e32 v2, vcc, 0x58000, v2
	s_nop 1
	v_addc_co_u32_e32 v3, vcc, 0, v3, vcc
	s_andn2_b64 vcc, exec, s[98:99]
	global_store_dwordx2 v[2:3], v[14:15], off
	s_cbranch_vccnz .LBB0_786
	s_branch .Lp6_entry_pre

.Lp7_entry_pre:
	s_andn2_b64 vcc, exec, s[14:15]
	s_cbranch_vccnz .Lp7_entry
	s_barrier

.LBB0_866:
	s_ashr_i32 s43, s42, 31
	s_lshl_b64 s[42:43], s[42:43], 13
	v_lshl_or_b32 v18, s40, 8, v212
	s_add_u32 s42, s56, s42
	s_addc_u32 s43, s57, s43
	v_ashrrev_i32_e32 v19, 31, v18
	v_lshl_add_u64 v[2:3], v[18:19], 2, s[42:43]
	global_load_dwordx4 v[10:13], v[2:3], off
	global_load_dwordx4 v[14:17], v[2:3], off offset:16
	global_load_dwordx4 v[192:195], v[2:3], off offset:512
	global_load_dwordx4 v[196:199], v[2:3], off offset:528
	v_lshl_add_u32 v20, s80, 8, v209
	v_ashrrev_i32_e32 v21, 31, v20
	v_or_b32_e32 v4, 16, v20
	v_or_b32_e32 v6, 32, v20
	v_lshlrev_b64 v[8:9], 11, v[20:21]
	v_ashrrev_i32_e32 v5, 31, v4
	v_ashrrev_i32_e32 v7, 31, v6
	v_lshl_add_u64 v[8:9], s[16:17], 0, v[8:9]
	v_lshlrev_b64 v[30:31], 11, v[4:5]
	v_lshlrev_b64 v[6:7], 11, v[6:7]
	v_lshl_add_u64 v[4:5], v[8:9], 0, v[18:19]
	v_lshl_add_u64 v[8:9], s[16:17], 0, v[30:31]
	v_lshl_add_u64 v[30:31], s[16:17], 0, v[6:7]
	v_lshl_add_u64 v[6:7], v[8:9], 0, v[18:19]
	v_lshl_add_u64 v[8:9], v[30:31], 0, v[18:19]
	v_mov_b32_e32 v22, 0
	v_mov_b32_e32 v23, 0
	v_mov_b32_e32 v24, 0
	v_mov_b32_e32 v25, 0
	v_mov_b32_e32 v26, 0
	v_mov_b32_e32 v27, 0
	v_mov_b32_e32 v28, 0
	s_mov_b64 s[98:99], s[0:1]
	s_andn2_b64 vcc, exec, s[0:1]
	s_cbranch_vccnz .Lp7u_done
	v_mov_b32_e32 v170, v219
	v_mov_b32_e32 v166, v218
	v_mov_b32_e32 v174, v217
	v_mov_b32_e32 v172, v216
	s_mov_b32 s42, s36
	s_mov_b32 s40, s34
	s_mov_b32 s80, s79
	s_mov_b64 s[44:45], s[38:39]
	s_add_i32 s64, s64, 1
	s_mul_i32 s0, s64, s65
	s_mul_hi_u32 s1, s64, s94
	s_add_i32 s1, s1, s0
	s_mul_i32 s0, s64, s94
	v_readlane_b32 s35, v254, 18
	s_add_u32 s46, s0, s35
	s_addc_u32 s47, s1, s52
	v_cmp_ge_i64_e32 vcc, s[46:47], v[168:169]
	v_cmp_lt_i64_e64 s[0:1], s[46:47], v[168:169]
	s_cbranch_vccnz .Lp7u_861
	s_ashr_i32 s34, s46, 31
	s_lshr_b32 s34, s34, 29
	s_add_i32 s34, s46, s34
	s_ashr_i32 s35, s34, 3
	s_and_b32 s34, s34, -8
	s_sub_i32 s34, s46, s34
	s_cmp_lt_i32 s34, 0
	s_cselect_b32 s36, s50, s23
	s_mul_i32 s34, s34, s36
	s_add_i32 s34, s34, s35
	s_ashr_i32 s35, s34, 31
	s_lshr_b32 s35, s35, 26
	s_add_i32 s35, s34, s35
	s_ashr_i32 s36, s35, 6
	s_lshl_b32 s36, s36, 3
	s_sub_i32 s37, s23, s36
	s_min_i32 s37, s37, 8
	s_abs_i32 s38, s37
	v_cvt_f32_u32_e32 v32, s38
	s_sub_i32 s43, 0, s38
	s_andn2_b32 s35, s35, 63
	s_sub_i32 s35, s34, s35
	v_rcp_iflag_f32_e32 v32, v32
	s_abs_i32 s34, s35
	s_xor_b32 s39, s35, s37
	s_ashr_i32 s39, s39, 31
	v_mul_f32_e32 v32, 0x4f7ffffe, v32
	v_cvt_u32_f32_e32 v32, v32
	s_nop 0
	v_readfirstlane_b32 s46, v32
	s_mul_i32 s43, s43, s46
	s_mul_hi_u32 s43, s46, s43
	s_add_i32 s46, s46, s43
	s_mul_hi_u32 s43, s34, s46
	s_mul_i32 s46, s43, s38
	s_sub_i32 s34, s34, s46
	s_add_i32 s47, s43, 1
	s_sub_i32 s46, s34, s38
	s_cmp_ge_u32 s34, s38
	s_cselect_b32 s43, s47, s43
	s_cselect_b32 s34, s46, s34
	s_add_i32 s46, s43, 1
	s_cmp_ge_u32 s34, s38
	s_cselect_b32 s34, s46, s43
	s_xor_b32 s34, s34, s39
	s_sub_i32 s34, s34, s39
	s_mul_i32 s37, s34, s37
	s_sub_i32 s35, s35, s37
	s_add_i32 s79, s36, s35
	s_add_i32 s35, s79, 0
	s_add_i32 s35, s35, 0x22200
	v_mov_b32_e32 v32, s35
	ds_read_u8 v32, v32
	s_waitcnt lgkmcnt(0)
	v_readfirstlane_b32 s36, v32
	s_ashr_i32 s37, s36, 31
	s_lshl_b64 s[38:39], s[36:37], 22
	s_add_u32 s37, s25, s38
	s_addc_u32 s43, s33, s39
	s_ashr_i32 s35, s34, 31
	s_lshl_b64 s[38:39], s[34:35], 19
	s_add_u32 s38, s37, s38
	s_addc_u32 s39, s43, s39
.Lp7u_861:
	s_lshl_b32 s37, s79, 8
	s_bitset1_b32 s37, 7
	s_lshl_b32 s35, s79, 19
	v_or_b32_e32 v32, s37, v1
	v_or_b32_e32 v176, s35, v207
	v_lshl_or_b32 v178, v32, 11, v204
	v_or_b32_e32 v180, s35, v208
	v_or_b32_e32 v32, s37, v205
	v_mov_b32_e32 v171, v167
	v_mov_b32_e32 v173, v167
	v_mov_b32_e32 v175, v167
	s_add_u32 s35, s44, 0x100
	v_lshl_or_b32 v182, v32, 11, v206
	v_mov_b32_e32 v177, v167
	v_mov_b32_e32 v181, v167
	v_mov_b32_e32 v179, v167
	v_mov_b32_e32 v183, v167
	v_lshl_add_u64 v[184:185], s[20:21], 0, v[174:175]
	v_lshl_add_u64 v[186:187], s[20:21], 0, v[172:173]
	v_lshl_add_u64 v[188:189], s[20:21], 0, v[170:171]
	v_lshl_add_u64 v[190:191], s[20:21], 0, v[166:167]
	s_addc_u32 s37, s45, 0
	s_mov_b32 s43, -2
	s_mov_b64 s[44:45], 0

.LBB0_868:
	s_nop 15
	s_nop 15
	s_waitcnt vmcnt(0)
	v_pk_mul_f32 v[30:31], v[10:11], s[22:23] op_sel_hi:[1,0]
	s_nop 0
	v_pk_fma_f32 v[32:33], v[158:159], s[24:25], v[30:31] op_sel_hi:[1,0,1]
	v_pk_mul_f32 v[12:13], v[12:13], s[22:23] op_sel_hi:[1,0]
	v_med3_f32 v21, v32, s74, v215
	v_med3_f32 v29, v33, s74, v215
	v_cvt_pk_fp8_f32 v22, v21, v29
	v_pk_mul_f32 v[14:15], v[14:15], s[22:23] op_sel_hi:[1,0]
	v_pk_fma_f32 v[10:11], v[160:161], s[24:25], v[12:13] op_sel_hi:[1,0,1]
	v_pk_fma_f32 v[130:131], v[130:131], s[24:25], v[14:15] op_sel_hi:[1,0,1]
	v_med3_f32 v10, v10, s74, v215
	v_med3_f32 v11, v11, s74, v215
	v_pk_fma_f32 v[154:155], v[154:155], s[24:25], v[14:15] op_sel_hi:[1,0,1]
	v_med3_f32 v130, v130, s74, v215
	v_cvt_pk_fp8_f32 v22, v10, v11 op_sel:[0,0,1]
	v_med3_f32 v10, v131, s74, v215
	v_mov_b32_e32 v29, 0
	v_pk_fma_f32 v[150:151], v[150:151], s[24:25], v[30:31] op_sel_hi:[1,0,1]
	v_pk_fma_f32 v[146:147], v[146:147], s[24:25], v[14:15] op_sel_hi:[1,0,1]
	v_med3_f32 v32, v154, s74, v215
	v_med3_f32 v33, v155, s74, v215
	v_cvt_pk_fp8_f32 v29, v130, v10
	v_pk_mul_f32 v[16:17], v[16:17], s[22:23] op_sel_hi:[1,0]
	v_pk_fma_f32 v[142:143], v[142:143], s[24:25], v[30:31] op_sel_hi:[1,0,1]
	v_pk_fma_f32 v[138:139], v[138:139], s[24:25], v[14:15] op_sel_hi:[1,0,1]
	v_med3_f32 v150, v150, s74, v215
	v_med3_f32 v151, v151, s74, v215
	v_med3_f32 v146, v146, s74, v215
	v_med3_f32 v147, v147, s74, v215
	v_cvt_pk_fp8_f32 v23, v32, v33
	v_pk_fma_f32 v[132:133], v[132:133], s[24:25], v[16:17] op_sel_hi:[1,0,1]
	v_med3_f32 v142, v142, s74, v215
	v_med3_f32 v143, v143, s74, v215
	v_med3_f32 v138, v138, s74, v215
	v_med3_f32 v139, v139, s74, v215
	v_cvt_pk_fp8_f32 v24, v150, v151
	v_cvt_pk_fp8_f32 v25, v146, v147
	v_pk_fma_f32 v[156:157], v[156:157], s[24:25], v[16:17] op_sel_hi:[1,0,1]
	v_cvt_pk_fp8_f32 v26, v142, v143
	v_cvt_pk_fp8_f32 v27, v138, v139
	v_med3_f32 v10, v132, s74, v215
	v_med3_f32 v11, v133, s74, v215
	v_pk_fma_f32 v[152:153], v[152:153], s[24:25], v[12:13] op_sel_hi:[1,0,1]
	v_pk_fma_f32 v[148:149], v[148:149], s[24:25], v[16:17] op_sel_hi:[1,0,1]
	v_med3_f32 v154, v156, s74, v215
	v_med3_f32 v155, v157, s74, v215
	v_cvt_pk_fp8_f32 v29, v10, v11 op_sel:[0,0,1]
	v_or_b32_e32 v10, 48, v20
	v_pk_fma_f32 v[144:145], v[144:145], s[24:25], v[12:13] op_sel_hi:[1,0,1]
	v_pk_fma_f32 v[140:141], v[140:141], s[24:25], v[16:17] op_sel_hi:[1,0,1]
	v_med3_f32 v152, v152, s74, v215
	v_med3_f32 v153, v153, s74, v215
	v_med3_f32 v148, v148, s74, v215
	v_med3_f32 v149, v149, s74, v215
	v_cvt_pk_fp8_f32 v23, v154, v155 op_sel:[0,0,1]
	v_ashrrev_i32_e32 v11, 31, v10
	v_med3_f32 v144, v144, s74, v215
	v_med3_f32 v145, v145, s74, v215
	v_med3_f32 v140, v140, s74, v215
	v_med3_f32 v141, v141, s74, v215
	v_cvt_pk_fp8_f32 v24, v152, v153 op_sel:[0,0,1]
	v_cvt_pk_fp8_f32 v25, v148, v149 op_sel:[0,0,1]
	v_lshlrev_b64 v[10:11], 11, v[10:11]
	v_cvt_pk_fp8_f32 v26, v144, v145 op_sel:[0,0,1]
	v_cvt_pk_fp8_f32 v27, v140, v141 op_sel:[0,0,1]
	v_lshl_add_u64 v[10:11], s[16:17], 0, v[10:11]
	v_lshl_add_u64 v[10:11], v[10:11], 0, v[18:19]
	v_pk_fma_f32 v[18:19], v[128:129], s[24:25], v[12:13] op_sel_hi:[1,0,1]
	v_pk_fma_f32 v[20:21], v[126:127], s[24:25], v[30:31] op_sel_hi:[1,0,1]
	global_store_dwordx2 v[4:5], v[22:23], off
	global_store_dwordx2 v[6:7], v[24:25], off
	global_store_dwordx2 v[8:9], v[26:27], off
	v_pk_fma_f32 v[24:25], v[122:123], s[24:25], v[14:15] op_sel_hi:[1,0,1]
	v_med3_f32 v20, v20, s74, v215
	v_med3_f32 v21, v21, s74, v215
	v_med3_f32 v26, v18, s74, v215
	v_mov_b32_e32 v18, 0
	v_med3_f32 v27, v19, s74, v215
	v_cvt_pk_fp8_f32 v18, v20, v21
	v_med3_f32 v20, v24, s74, v215
	v_med3_f32 v21, v25, s74, v215
	v_mov_b32_e32 v19, 0
	v_cvt_pk_fp8_f32 v19, v20, v21
	v_pk_fma_f32 v[22:23], v[124:125], s[24:25], v[16:17] op_sel_hi:[1,0,1]
	v_cvt_pk_fp8_f32 v18, v26, v27 op_sel:[0,0,1]
	v_med3_f32 v20, v22, s74, v215
	v_med3_f32 v21, v23, s74, v215
	v_cvt_pk_fp8_f32 v19, v20, v21 op_sel:[0,0,1]
	v_add_co_u32_e32 v20, vcc, s75, v4
	v_pk_fma_f32 v[24:25], v[114:115], s[24:25], v[14:15] op_sel_hi:[1,0,1]
	s_nop 0
	v_addc_co_u32_e32 v21, vcc, 0, v5, vcc
	global_store_dwordx2 v[20:21], v[18:19], off
	v_pk_fma_f32 v[18:19], v[120:121], s[24:25], v[12:13] op_sel_hi:[1,0,1]
	v_pk_fma_f32 v[20:21], v[118:119], s[24:25], v[30:31] op_sel_hi:[1,0,1]
	v_med3_f32 v26, v18, s74, v215
	v_med3_f32 v20, v20, s74, v215
	v_med3_f32 v21, v21, s74, v215
	v_mov_b32_e32 v18, 0
	v_med3_f32 v27, v19, s74, v215
	v_cvt_pk_fp8_f32 v18, v20, v21
	v_med3_f32 v20, v24, s74, v215
	v_med3_f32 v21, v25, s74, v215
	v_mov_b32_e32 v19, 0
	v_cvt_pk_fp8_f32 v19, v20, v21
	v_pk_fma_f32 v[22:23], v[116:117], s[24:25], v[16:17] op_sel_hi:[1,0,1]
	v_cvt_pk_fp8_f32 v18, v26, v27 op_sel:[0,0,1]
	v_med3_f32 v20, v22, s74, v215
	v_med3_f32 v21, v23, s74, v215
	v_cvt_pk_fp8_f32 v19, v20, v21 op_sel:[0,0,1]
	v_add_co_u32_e32 v20, vcc, s76, v4
	v_pk_fma_f32 v[24:25], v[106:107], s[24:25], v[14:15] op_sel_hi:[1,0,1]
	s_nop 0
	v_addc_co_u32_e32 v21, vcc, 0, v5, vcc
	global_store_dwordx2 v[20:21], v[18:19], off
	v_pk_fma_f32 v[18:19], v[112:113], s[24:25], v[12:13] op_sel_hi:[1,0,1]
	v_pk_fma_f32 v[20:21], v[110:111], s[24:25], v[30:31] op_sel_hi:[1,0,1]
	v_med3_f32 v26, v18, s74, v215
	v_med3_f32 v20, v20, s74, v215
	v_med3_f32 v21, v21, s74, v215
	v_mov_b32_e32 v18, 0
	v_med3_f32 v27, v19, s74, v215
	v_cvt_pk_fp8_f32 v18, v20, v21
	v_med3_f32 v20, v24, s74, v215
	v_med3_f32 v21, v25, s74, v215
	v_mov_b32_e32 v19, 0
	v_cvt_pk_fp8_f32 v19, v20, v21
	v_pk_fma_f32 v[22:23], v[108:109], s[24:25], v[16:17] op_sel_hi:[1,0,1]
	v_cvt_pk_fp8_f32 v18, v26, v27 op_sel:[0,0,1]
	v_med3_f32 v20, v22, s74, v215
	v_med3_f32 v21, v23, s74, v215
	v_cvt_pk_fp8_f32 v19, v20, v21 op_sel:[0,0,1]
	v_add_co_u32_e32 v20, vcc, s77, v4
	v_pk_fma_f32 v[136:137], v[136:137], s[24:25], v[12:13] op_sel_hi:[1,0,1]
	s_nop 0
	v_addc_co_u32_e32 v21, vcc, 0, v5, vcc
	v_pk_fma_f32 v[134:135], v[134:135], s[24:25], v[30:31] op_sel_hi:[1,0,1]
	global_store_dwordx2 v[20:21], v[18:19], off
	v_pk_fma_f32 v[12:13], v[100:101], s[24:25], v[12:13] op_sel_hi:[1,0,1]
	v_pk_fma_f32 v[18:19], v[98:99], s[24:25], v[30:31] op_sel_hi:[1,0,1]
	v_pk_fma_f32 v[14:15], v[90:91], s[24:25], v[14:15] op_sel_hi:[1,0,1]
	v_med3_f32 v134, v134, s74, v215
	v_med3_f32 v135, v135, s74, v215
	v_med3_f32 v18, v18, s74, v215
	v_med3_f32 v19, v19, s74, v215
	v_med3_f32 v20, v12, s74, v215
	v_med3_f32 v21, v13, s74, v215
	v_mov_b32_e32 v12, 0
	v_med3_f32 v14, v14, s74, v215
	v_med3_f32 v15, v15, s74, v215
	v_mov_b32_e32 v13, 0
	v_cvt_pk_fp8_f32 v28, v134, v135
	v_cvt_pk_fp8_f32 v12, v18, v19
	v_cvt_pk_fp8_f32 v13, v14, v15
	v_pk_fma_f32 v[16:17], v[92:93], s[24:25], v[16:17] op_sel_hi:[1,0,1]
	v_med3_f32 v136, v136, s74, v215
	v_med3_f32 v137, v137, s74, v215
	v_med3_f32 v14, v16, s74, v215
	v_med3_f32 v15, v17, s74, v215
	v_cvt_pk_fp8_f32 v28, v136, v137 op_sel:[0,0,1]
	v_cvt_pk_fp8_f32 v12, v20, v21 op_sel:[0,0,1]
	v_cvt_pk_fp8_f32 v13, v14, v15 op_sel:[0,0,1]
	v_add_co_u32_e32 v14, vcc, s78, v4
	global_store_dwordx2 v[10:11], v[28:29], off
	s_nop 0
	v_addc_co_u32_e32 v15, vcc, 0, v5, vcc
	global_store_dwordx2 v[14:15], v[12:13], off
	v_lshl_add_u64 v[2:3], v[4:5], 0, s[12:13]
	v_lshl_add_u64 v[20:21], v[4:5], 0, s[26:27]
	v_lshl_add_u64 v[22:23], v[4:5], 0, s[28:29]
	v_lshl_add_u64 v[24:25], v[4:5], 0, s[30:31]
	s_andn2_b64 vcc, exec, s[98:99]
	v_pk_mul_f32 v[14:15], v[194:195], s[22:23] op_sel_hi:[1,0]
	v_pk_mul_f32 v[12:13], v[192:193], s[22:23] op_sel_hi:[1,0]
	v_pk_mul_f32 v[16:17], v[196:197], s[22:23] op_sel_hi:[1,0]
	v_pk_fma_f32 v[26:27], v[104:105], s[24:25], v[14:15] op_sel_hi:[1,0,1]
	v_pk_fma_f32 v[28:29], v[102:103], s[24:25], v[12:13] op_sel_hi:[1,0,1]
	v_pk_fma_f32 v[32:33], v[94:95], s[24:25], v[16:17] op_sel_hi:[1,0,1]
	v_med3_f32 v28, v28, s74, v215
	v_med3_f32 v29, v29, s74, v215
	v_med3_f32 v90, v26, s74, v215
	v_mov_b32_e32 v26, 0
	v_med3_f32 v91, v27, s74, v215
	v_cvt_pk_fp8_f32 v26, v28, v29
	v_med3_f32 v28, v32, s74, v215
	v_med3_f32 v29, v33, s74, v215
	v_mov_b32_e32 v27, 0
	v_cvt_pk_fp8_f32 v27, v28, v29
	v_pk_mul_f32 v[18:19], v[198:199], s[22:23] op_sel_hi:[1,0]
	v_pk_fma_f32 v[82:83], v[82:83], s[24:25], v[16:17] op_sel_hi:[1,0,1]
	v_pk_fma_f32 v[30:31], v[96:97], s[24:25], v[18:19] op_sel_hi:[1,0,1]
	v_pk_fma_f32 v[32:33], v[84:85], s[24:25], v[18:19] op_sel_hi:[1,0,1]
	v_med3_f32 v28, v30, s74, v215
	v_med3_f32 v29, v31, s74, v215
	v_cvt_pk_fp8_f32 v27, v28, v29 op_sel:[0,0,1]
	v_pk_fma_f32 v[28:29], v[88:89], s[24:25], v[14:15] op_sel_hi:[1,0,1]
	v_pk_fma_f32 v[30:31], v[86:87], s[24:25], v[12:13] op_sel_hi:[1,0,1]
	v_med3_f32 v84, v28, s74, v215
	v_med3_f32 v30, v30, s74, v215
	v_med3_f32 v31, v31, s74, v215
	v_mov_b32_e32 v28, 0
	v_med3_f32 v85, v29, s74, v215
	v_cvt_pk_fp8_f32 v28, v30, v31
	v_med3_f32 v30, v82, s74, v215
	v_med3_f32 v31, v83, s74, v215
	v_mov_b32_e32 v29, 0
	v_cvt_pk_fp8_f32 v29, v30, v31
	v_med3_f32 v30, v32, s74, v215
	v_med3_f32 v31, v33, s74, v215
	v_pk_fma_f32 v[32:33], v[78:79], s[24:25], v[12:13] op_sel_hi:[1,0,1]
	v_cvt_pk_fp8_f32 v29, v30, v31 op_sel:[0,0,1]
	v_pk_fma_f32 v[30:31], v[80:81], s[24:25], v[14:15] op_sel_hi:[1,0,1]
	v_pk_fma_f32 v[74:75], v[74:75], s[24:25], v[16:17] op_sel_hi:[1,0,1]
	v_med3_f32 v32, v32, s74, v215
	v_med3_f32 v33, v33, s74, v215
	v_med3_f32 v78, v30, s74, v215
	v_mov_b32_e32 v30, 0
	v_med3_f32 v79, v31, s74, v215
	v_cvt_pk_fp8_f32 v30, v32, v33
	v_med3_f32 v32, v74, s74, v215
	v_med3_f32 v33, v75, s74, v215
	v_mov_b32_e32 v31, 0
	v_cvt_pk_fp8_f32 v31, v32, v33
	v_pk_fma_f32 v[76:77], v[76:77], s[24:25], v[18:19] op_sel_hi:[1,0,1]
	v_pk_fma_f32 v[70:71], v[70:71], s[24:25], v[12:13] op_sel_hi:[1,0,1]
	v_med3_f32 v32, v76, s74, v215
	v_med3_f32 v33, v77, s74, v215
	v_cvt_pk_fp8_f32 v31, v32, v33 op_sel:[0,0,1]
	v_pk_fma_f32 v[32:33], v[72:73], s[24:25], v[14:15] op_sel_hi:[1,0,1]
	v_pk_fma_f32 v[66:67], v[66:67], s[24:25], v[16:17] op_sel_hi:[1,0,1]
	v_med3_f32 v70, v70, s74, v215
	v_med3_f32 v71, v71, s74, v215
	v_med3_f32 v72, v32, s74, v215
	v_med3_f32 v73, v33, s74, v215
	v_mov_b32_e32 v32, 0
	v_med3_f32 v66, v66, s74, v215
	v_med3_f32 v67, v67, s74, v215
	v_mov_b32_e32 v33, 0
	v_cvt_pk_fp8_f32 v32, v70, v71
	v_cvt_pk_fp8_f32 v33, v66, v67
	v_cvt_pk_fp8_f32 v26, v90, v91 op_sel:[0,0,1]
	v_cvt_pk_fp8_f32 v28, v84, v85 op_sel:[0,0,1]
	v_pk_fma_f32 v[68:69], v[68:69], s[24:25], v[18:19] op_sel_hi:[1,0,1]
	v_cvt_pk_fp8_f32 v30, v78, v79 op_sel:[0,0,1]
	v_med3_f32 v66, v68, s74, v215
	v_med3_f32 v67, v69, s74, v215
	v_cvt_pk_fp8_f32 v32, v72, v73 op_sel:[0,0,1]
	v_cvt_pk_fp8_f32 v33, v66, v67 op_sel:[0,0,1]
	global_store_dwordx2 v[4:5], v[26:27], off offset:128
	global_store_dwordx2 v[6:7], v[28:29], off offset:128
	global_store_dwordx2 v[8:9], v[30:31], off offset:128
	global_store_dwordx2 v[10:11], v[32:33], off offset:128
	v_pk_fma_f32 v[4:5], v[64:65], s[24:25], v[14:15] op_sel_hi:[1,0,1]
	v_pk_fma_f32 v[6:7], v[62:63], s[24:25], v[12:13] op_sel_hi:[1,0,1]
	v_pk_fma_f32 v[10:11], v[58:59], s[24:25], v[16:17] op_sel_hi:[1,0,1]
	v_med3_f32 v6, v6, s74, v215
	v_med3_f32 v7, v7, s74, v215
	v_med3_f32 v26, v4, s74, v215
	v_mov_b32_e32 v4, 0
	v_med3_f32 v27, v5, s74, v215
	v_cvt_pk_fp8_f32 v4, v6, v7
	v_med3_f32 v6, v10, s74, v215
	v_med3_f32 v7, v11, s74, v215
	v_mov_b32_e32 v5, 0
	v_cvt_pk_fp8_f32 v5, v6, v7
	v_pk_fma_f32 v[8:9], v[60:61], s[24:25], v[18:19] op_sel_hi:[1,0,1]
	v_cvt_pk_fp8_f32 v4, v26, v27 op_sel:[0,0,1]
	v_med3_f32 v6, v8, s74, v215
	v_med3_f32 v7, v9, s74, v215
	v_cvt_pk_fp8_f32 v5, v6, v7 op_sel:[0,0,1]
	v_pk_fma_f32 v[6:7], v[56:57], s[24:25], v[14:15] op_sel_hi:[1,0,1]
	v_pk_fma_f32 v[8:9], v[54:55], s[24:25], v[12:13] op_sel_hi:[1,0,1]
	v_pk_fma_f32 v[26:27], v[50:51], s[24:25], v[16:17] op_sel_hi:[1,0,1]
	v_med3_f32 v8, v8, s74, v215
	v_med3_f32 v9, v9, s74, v215
	v_med3_f32 v28, v6, s74, v215
	v_mov_b32_e32 v6, 0
	v_med3_f32 v29, v7, s74, v215
	v_cvt_pk_fp8_f32 v6, v8, v9
	v_med3_f32 v8, v26, s74, v215
	v_med3_f32 v9, v27, s74, v215
	v_mov_b32_e32 v7, 0
	v_cvt_pk_fp8_f32 v7, v8, v9
	v_pk_fma_f32 v[10:11], v[52:53], s[24:25], v[18:19] op_sel_hi:[1,0,1]
	v_cvt_pk_fp8_f32 v6, v28, v29 op_sel:[0,0,1]
	v_med3_f32 v8, v10, s74, v215
	v_med3_f32 v9, v11, s74, v215
	v_cvt_pk_fp8_f32 v7, v8, v9 op_sel:[0,0,1]
	v_pk_fma_f32 v[8:9], v[48:49], s[24:25], v[14:15] op_sel_hi:[1,0,1]
	v_pk_fma_f32 v[10:11], v[46:47], s[24:25], v[12:13] op_sel_hi:[1,0,1]
	v_pk_fma_f32 v[28:29], v[42:43], s[24:25], v[16:17] op_sel_hi:[1,0,1]
	v_med3_f32 v10, v10, s74, v215
	v_med3_f32 v11, v11, s74, v215
	v_med3_f32 v30, v8, s74, v215
	v_mov_b32_e32 v8, 0
	v_med3_f32 v31, v9, s74, v215
	v_cvt_pk_fp8_f32 v8, v10, v11
	v_med3_f32 v10, v28, s74, v215
	v_med3_f32 v11, v29, s74, v215
	v_mov_b32_e32 v9, 0
	v_cvt_pk_fp8_f32 v9, v10, v11
	v_pk_fma_f32 v[26:27], v[44:45], s[24:25], v[18:19] op_sel_hi:[1,0,1]
	v_pk_fma_f32 v[12:13], v[38:39], s[24:25], v[12:13] op_sel_hi:[1,0,1]
	v_med3_f32 v10, v26, s74, v215
	v_med3_f32 v11, v27, s74, v215
	v_cvt_pk_fp8_f32 v9, v10, v11 op_sel:[0,0,1]
	v_pk_fma_f32 v[10:11], v[40:41], s[24:25], v[14:15] op_sel_hi:[1,0,1]
	v_pk_fma_f32 v[14:15], v[36:37], s[24:25], v[18:19] op_sel_hi:[1,0,1]
	v_pk_fma_f32 v[16:17], v[34:35], s[24:25], v[16:17] op_sel_hi:[1,0,1]
	v_med3_f32 v12, v12, s74, v215
	v_med3_f32 v13, v13, s74, v215
	v_med3_f32 v18, v10, s74, v215
	v_mov_b32_e32 v10, 0
	v_med3_f32 v19, v11, s74, v215
	v_cvt_pk_fp8_f32 v10, v12, v13
	v_med3_f32 v12, v16, s74, v215
	v_med3_f32 v13, v17, s74, v215
	v_mov_b32_e32 v11, 0
	v_cvt_pk_fp8_f32 v11, v12, v13
	v_cvt_pk_fp8_f32 v8, v30, v31 op_sel:[0,0,1]
	v_med3_f32 v12, v14, s74, v215
	v_med3_f32 v13, v15, s74, v215
	v_cvt_pk_fp8_f32 v10, v18, v19 op_sel:[0,0,1]
	v_cvt_pk_fp8_f32 v11, v12, v13 op_sel:[0,0,1]
	global_store_dwordx2 v[2:3], v[4:5], off offset:128
	global_store_dwordx2 v[20:21], v[6:7], off offset:128
	global_store_dwordx2 v[22:23], v[8:9], off offset:128
	global_store_dwordx2 v[24:25], v[10:11], off offset:128
	s_cbranch_vccnz .LBB0_871
	s_branch .Lp7_entry_pre

	.amdhsa_kernel _ZN12_GLOBAL__N_16mk_fwdENS_4ArgsE
		.amdhsa_group_segment_fixed_size 0
		.amdhsa_private_segment_fixed_size 0
		.amdhsa_kernarg_size 464
		.amdhsa_user_sgpr_count 2
		.amdhsa_user_sgpr_dispatch_ptr 0
		.amdhsa_user_sgpr_queue_ptr 0
		.amdhsa_user_sgpr_kernarg_segment_ptr 1
		.amdhsa_user_sgpr_dispatch_id 0
		.amdhsa_user_sgpr_kernarg_preload_length 0
		.amdhsa_user_sgpr_kernarg_preload_offset 0
		.amdhsa_user_sgpr_private_segment_size 0
		.amdhsa_uses_dynamic_stack 0
		.amdhsa_enable_private_segment 0
		.amdhsa_system_sgpr_workgroup_id_x 1
		.amdhsa_system_sgpr_workgroup_id_y 0
		.amdhsa_system_sgpr_workgroup_id_z 0
		.amdhsa_system_sgpr_workgroup_info 0
		.amdhsa_system_vgpr_workitem_id 0
		.amdhsa_next_free_vgpr 256
		.amdhsa_next_free_sgpr 100
		.amdhsa_accum_offset 256
		.amdhsa_reserve_vcc 1
		.amdhsa_float_round_mode_32 0
		.amdhsa_float_round_mode_16_64 0
		.amdhsa_float_denorm_mode_32 3
		.amdhsa_float_denorm_mode_16_64 3
		.amdhsa_dx10_clamp 1
		.amdhsa_ieee_mode 1
		.amdhsa_fp16_overflow 0
		.amdhsa_tg_split 0
		.amdhsa_exception_fp_ieee_invalid_op 0
		.amdhsa_exception_fp_denorm_src 0
		.amdhsa_exception_fp_ieee_div_zero 0
		.amdhsa_exception_fp_ieee_overflow 0
		.amdhsa_exception_fp_ieee_underflow 0
		.amdhsa_exception_fp_ieee_inexact 0
		.amdhsa_exception_int_div_zero 0
	.end_amdhsa_kernel

amdhsa.kernels:
  - .agpr_count:     0
    .args:
      - .offset:         0
        .size:           208
        .value_kind:     by_value
      - .offset:         208
        .size:           4
        .value_kind:     hidden_block_count_x
      - .offset:         212
        .size:           4
        .value_kind:     hidden_block_count_y
      - .offset:         216
        .size:           4
        .value_kind:     hidden_block_count_z
      - .offset:         220
        .size:           2
        .value_kind:     hidden_group_size_x
      - .offset:         222
        .size:           2
        .value_kind:     hidden_group_size_y
      - .offset:         224
        .size:           2
        .value_kind:     hidden_group_size_z
      - .offset:         226
        .size:           2
        .value_kind:     hidden_remainder_x
      - .offset:         228
        .size:           2
        .value_kind:     hidden_remainder_y
      - .offset:         230
        .size:           2
        .value_kind:     hidden_remainder_z
      - .offset:         248
        .size:           8
        .value_kind:     hidden_global_offset_x
      - .offset:         256
        .size:           8
        .value_kind:     hidden_global_offset_y
      - .offset:         264
        .size:           8
        .value_kind:     hidden_global_offset_z
      - .offset:         272
        .size:           2
        .value_kind:     hidden_grid_dims
      - .offset:         328
        .size:           4
        .value_kind:     hidden_dynamic_lds_size
    .group_segment_fixed_size: 0
    .kernarg_segment_align: 8
    .kernarg_segment_size: 464
    .language:       OpenCL C
    .language_version:
      - 2
      - 0
    .max_flat_workgroup_size: 512
    .name:           _ZN12_GLOBAL__N_16mk_fwdENS_4ArgsE
    .private_segment_fixed_size: 0
    .sgpr_count:     106
    .sgpr_spill_count: 109
    .symbol:         _ZN12_GLOBAL__N_16mk_fwdENS_4ArgsE.kd
    .uniform_work_group_size: 1
    .uses_dynamic_stack: false
    .vgpr_count:     256
    .vgpr_spill_count: 0
    .wavefront_size: 64
